# HGRN step D (Lever 1): the VMEM waits left over from the hoisted rec_g loads moved to their only remaining consumer, the gate-register rotation at the loop tail
# speedup vs baseline: 1.0116x; 1.0005x over previous
.LBB0_666:
	ds_read_b64_tr_b16 v[78:79], v157 offset:53248
	ds_read_b64_tr_b16 v[80:81], v157 offset:54400
	ds_read_b64_tr_b16 v[74:75], v157 offset:62464
	ds_read_b64_tr_b16 v[76:77], v157 offset:63616
	ds_read_b128 v[82:85], v158
	ds_read_b128 v[86:89], v158 offset:2304
	ds_read_b128 v[90:93], v158 offset:4608
	ds_read_b128 v[94:97], v158 offset:4672
	ds_read_b128 v[98:101], v158 offset:6976
	v_add_u32_e32 v108, v137, v135
	v_add_u32_e32 v104, v137, v141
	s_waitcnt lgkmcnt(4)
	v_mfma_f32_16x16x32_bf16 v[82:85], v[82:85], v[78:81], 0
	v_add_u32_e32 v122, v142, v135
	v_add_u32_e32 v123, v143, v135
	v_add_u32_e32 v171, v144, v135
	s_waitcnt lgkmcnt(2)
	v_mfma_f32_16x16x32_bf16 v[90:93], v[90:93], v[78:81], 0
	s_lshl_b32 s30, s49, 6
	s_add_i32 s49, s49, 1
	s_add_u32 s38, s38, 0x240000
	s_waitcnt lgkmcnt(1)
	v_mfma_f32_16x16x32_bf16 v[90:93], v[94:97], v[74:77], v[90:93]
	ds_read_b128 v[94:97], v158 offset:6912
	s_addc_u32 s39, s39, 0
	s_mov_b64 s[26:27], 0x20000
	v_mfma_f32_16x16x32_bf16 v[86:89], v[86:89], v[78:81], 0
	v_lshl_add_u64 v[120:121], v[120:121], 0, s[26:27]
	s_cmp_lg_u32 s38, 0x4800000
	s_waitcnt lgkmcnt(0)
	v_mfma_f32_16x16x32_bf16 v[94:97], v[94:97], v[78:81], 0
	v_mfma_f32_16x16x32_bf16 v[94:97], v[98:101], v[74:77], v[94:97]
	v_cvt_pk_bf16_f32 v98, v26, v27
	v_cvt_pk_bf16_f32 v99, v28, v29
	v_cvt_pk_bf16_f32 v100, v30, v31
	v_cvt_pk_bf16_f32 v101, v32, v33
	ds_read_b64 v[102:103], v108
	ds_read_b64 v[104:105], v104
	s_waitcnt lgkmcnt(0)
	v_mfma_f32_16x16x32_bf16 v[82:85], v[102:105], v[98:101], v[82:85]
	v_add_u32_e32 v104, v142, v141
	ds_read_b64 v[102:103], v122
	ds_read_b64 v[104:105], v104
	s_waitcnt lgkmcnt(0)
	v_mfma_f32_16x16x32_bf16 v[86:89], v[102:105], v[98:101], v[86:89]
	v_add_u32_e32 v104, v143, v141
	ds_read_b64 v[102:103], v123
	ds_read_b64 v[104:105], v104
	s_waitcnt lgkmcnt(0)
	v_mfma_f32_16x16x32_bf16 v[90:93], v[102:105], v[98:101], v[90:93]
	v_add_u32_e32 v104, v144, v141
	ds_read_b64 v[102:103], v171
	ds_read_b64 v[104:105], v104
	s_waitcnt lgkmcnt(0)
	v_mfma_f32_16x16x32_bf16 v[94:97], v[102:105], v[98:101], v[94:97]
	v_add_u32_e32 v102, v137, v145
	v_add_u32_e32 v104, v137, v146
	v_cvt_pk_bf16_f32 v98, v62, v63
	v_cvt_pk_bf16_f32 v99, v64, v65
	v_cvt_pk_bf16_f32 v100, v54, v55
	v_cvt_pk_bf16_f32 v101, v56, v57
	ds_read_b64 v[102:103], v102
	ds_read_b64 v[104:105], v104
	s_waitcnt lgkmcnt(0)
	v_mfma_f32_16x16x32_bf16 v[82:85], v[102:105], v[98:101], v[82:85]
	v_add_u32_e32 v102, v142, v145
	v_add_u32_e32 v104, v142, v146
	ds_read_b64 v[102:103], v102
	ds_read_b64 v[104:105], v104
	s_waitcnt lgkmcnt(0)
	v_mfma_f32_16x16x32_bf16 v[86:89], v[102:105], v[98:101], v[86:89]
	v_add_u32_e32 v102, v143, v145
	v_add_u32_e32 v104, v143, v146
	ds_read_b64 v[102:103], v102
	ds_read_b64 v[104:105], v104
	s_waitcnt lgkmcnt(0)
	v_mfma_f32_16x16x32_bf16 v[90:93], v[102:105], v[98:101], v[90:93]
	v_add_u32_e32 v102, v144, v145
	v_add_u32_e32 v104, v144, v146
	ds_read_b64 v[102:103], v102
	ds_read_b64 v[104:105], v104
	s_waitcnt lgkmcnt(0)
	v_mfma_f32_16x16x32_bf16 v[94:97], v[102:105], v[98:101], v[94:97]
	v_cvt_pk_bf16_f32 v98, v34, v35
	v_cvt_pk_bf16_f32 v99, v36, v37
	v_cvt_pk_bf16_f32 v100, v50, v51
	v_cvt_pk_bf16_f32 v101, v52, v53
	ds_read2_b64 v[102:105], v108 offset0:16 offset1:20
	s_waitcnt lgkmcnt(0)
	v_mfma_f32_16x16x32_bf16 v[82:85], v[102:105], v[98:101], v[82:85]
	ds_read2_b64 v[102:105], v122 offset0:16 offset1:20
	s_waitcnt lgkmcnt(0)
	v_mfma_f32_16x16x32_bf16 v[86:89], v[102:105], v[98:101], v[86:89]
	ds_read2_b64 v[102:105], v123 offset0:16 offset1:20
	s_waitcnt lgkmcnt(0)
	v_mfma_f32_16x16x32_bf16 v[90:93], v[102:105], v[98:101], v[90:93]
	ds_read2_b64 v[102:105], v171 offset0:16 offset1:20
	s_waitcnt lgkmcnt(0)
	v_mfma_f32_16x16x32_bf16 v[94:97], v[102:105], v[98:101], v[94:97]
	v_cvt_pk_bf16_f32 v98, v42, v43
	v_cvt_pk_bf16_f32 v99, v44, v45
	v_cvt_pk_bf16_f32 v100, v58, v59
	v_cvt_pk_bf16_f32 v101, v60, v61
	ds_read2_b64 v[102:105], v108 offset0:24 offset1:28
	s_waitcnt lgkmcnt(0)
	v_mfma_f32_16x16x32_bf16 v[82:85], v[102:105], v[98:101], v[82:85]
	ds_read2_b64 v[102:105], v122 offset0:24 offset1:28
	s_waitcnt lgkmcnt(0)
	v_mfma_f32_16x16x32_bf16 v[86:89], v[102:105], v[98:101], v[86:89]
	ds_read2_b64 v[102:105], v123 offset0:24 offset1:28
	v_lshl_add_u64 v[122:123], v[118:119], 0, s[30:31]
	s_waitcnt lgkmcnt(0)
	v_mfma_f32_16x16x32_bf16 v[90:93], v[102:105], v[98:101], v[90:93]
	ds_read2_b64 v[102:105], v171 offset0:24 offset1:28
	ds_write2_b32 v159, v82, v83 offset1:132
	v_add_u32_e32 v82, 0x400, v159
	s_waitcnt lgkmcnt(1)
	v_mfma_f32_16x16x32_bf16 v[94:97], v[102:105], v[98:101], v[94:97]
	ds_write2_b32 v82, v84, v85 offset0:8 offset1:140
	ds_write_b32 v160, v86
	v_add_u32_e32 v82, 0x2200, v159
	ds_write2_b32 v82, v87, v88 offset0:68 offset1:200
	ds_write_b32 v159, v89 offset:10032
	ds_write_b32 v160, v90 offset:8448
	v_add_u32_e32 v82, 0x4400, v159
	ds_write2_b32 v82, v91, v92 offset0:4 offset1:136
	ds_write_b32 v159, v93 offset:18480
	ds_write_b32 v160, v94 offset:16896
	v_add_u32_e32 v82, 0x6400, v159
	ds_write2_b32 v82, v95, v96 offset0:68 offset1:200
	ds_write_b32 v159, v97 offset:26928
	v_add_u32_e32 v92, 0x1c000, v134
	ds_read_b128 v[82:85], v92
	s_waitcnt lgkmcnt(0)
	v_pk_mul_f32 v[26:27], v[26:27], v[82:83]
	v_add_u32_e32 v82, v140, v136
	v_pk_mul_f32 v[28:29], v[28:29], v[84:85]
	ds_read_b64_tr_b16 v[86:87], v82 offset:35968
	ds_read_b64_tr_b16 v[84:85], v82 offset:34816
	ds_read_b64_tr_b16 v[88:89], v82 offset:34848
	s_waitcnt lgkmcnt(1)
	v_mfma_f32_16x16x32_bf16 v[26:29], v[84:87], v[78:81], v[26:29]
	ds_read_b64_tr_b16 v[84:85], v82 offset:44032
	ds_read_b64_tr_b16 v[86:87], v82 offset:45184
	ds_read_b64_tr_b16 v[90:91], v82 offset:36000
	s_waitcnt lgkmcnt(1)
	v_mfma_f32_16x16x32_bf16 v[26:29], v[84:87], v[74:77], v[26:29]
	ds_read_b128 v[84:87], v92 offset:64
	s_waitcnt lgkmcnt(0)
	v_pk_mul_f32 v[30:31], v[30:31], v[84:85]
	v_pk_mul_f32 v[32:33], v[32:33], v[86:87]
	ds_read_b64_tr_b16 v[84:85], v82 offset:44064
	ds_read_b64_tr_b16 v[86:87], v82 offset:45216
	v_mfma_f32_16x16x32_bf16 v[30:33], v[88:91], v[78:81], v[30:33]
	s_waitcnt lgkmcnt(0)
	v_mfma_f32_16x16x32_bf16 v[30:33], v[84:87], v[74:77], v[30:33]
	ds_read_b128 v[84:87], v92 offset:128
	s_waitcnt lgkmcnt(0)
	v_pk_mul_f32 v[62:63], v[62:63], v[84:85]
	v_pk_mul_f32 v[64:65], v[64:65], v[86:87]
	ds_read_b64_tr_b16 v[84:85], v82 offset:34880
	ds_read_b64_tr_b16 v[86:87], v82 offset:36032
	s_waitcnt lgkmcnt(0)
	v_mfma_f32_16x16x32_bf16 v[62:65], v[84:87], v[78:81], v[62:65]
	ds_read_b64_tr_b16 v[84:85], v82 offset:44096
	ds_read_b64_tr_b16 v[86:87], v82 offset:45248
	s_waitcnt lgkmcnt(0)
	v_mfma_f32_16x16x32_bf16 v[62:65], v[84:87], v[74:77], v[62:65]
	ds_read_b128 v[84:87], v92 offset:192
	s_waitcnt lgkmcnt(0)
	v_pk_mul_f32 v[54:55], v[54:55], v[84:85]
	v_pk_mul_f32 v[56:57], v[56:57], v[86:87]
	ds_read_b64_tr_b16 v[84:85], v82 offset:34912
	ds_read_b64_tr_b16 v[86:87], v82 offset:36064
	s_waitcnt lgkmcnt(0)
	v_mfma_f32_16x16x32_bf16 v[54:57], v[84:87], v[78:81], v[54:57]
	ds_read_b64_tr_b16 v[84:85], v82 offset:44128
	ds_read_b64_tr_b16 v[86:87], v82 offset:45280
	s_waitcnt lgkmcnt(0)
	v_mfma_f32_16x16x32_bf16 v[54:57], v[84:87], v[74:77], v[54:57]
	ds_read_b128 v[84:87], v92 offset:256
	s_waitcnt lgkmcnt(0)
	v_pk_mul_f32 v[34:35], v[34:35], v[84:85]
	v_pk_mul_f32 v[36:37], v[36:37], v[86:87]
	ds_read_b64_tr_b16 v[84:85], v82 offset:34944
	ds_read_b64_tr_b16 v[86:87], v82 offset:36096
	s_waitcnt lgkmcnt(0)
	v_mfma_f32_16x16x32_bf16 v[34:37], v[84:87], v[78:81], v[34:37]
	ds_read_b64_tr_b16 v[84:85], v82 offset:44160
	ds_read_b64_tr_b16 v[86:87], v82 offset:45312
	s_waitcnt lgkmcnt(0)
	v_mfma_f32_16x16x32_bf16 v[34:37], v[84:87], v[74:77], v[34:37]
	ds_read_b128 v[84:87], v92 offset:320
	s_waitcnt lgkmcnt(0)
	v_pk_mul_f32 v[50:51], v[50:51], v[84:85]
	v_pk_mul_f32 v[52:53], v[52:53], v[86:87]
	ds_read_b64_tr_b16 v[84:85], v82 offset:34976
	ds_read_b64_tr_b16 v[86:87], v82 offset:36128
	s_waitcnt lgkmcnt(0)
	v_mfma_f32_16x16x32_bf16 v[50:53], v[84:87], v[78:81], v[50:53]
	ds_read_b64_tr_b16 v[84:85], v82 offset:44192
	ds_read_b64_tr_b16 v[86:87], v82 offset:45344
	s_waitcnt lgkmcnt(0)
	v_mfma_f32_16x16x32_bf16 v[50:53], v[84:87], v[74:77], v[50:53]
	ds_read_b128 v[84:87], v92 offset:384
	s_waitcnt lgkmcnt(0)
	v_pk_mul_f32 v[42:43], v[42:43], v[84:85]
	v_pk_mul_f32 v[44:45], v[44:45], v[86:87]
	ds_read_b64_tr_b16 v[84:85], v82 offset:35008
	ds_read_b64_tr_b16 v[86:87], v82 offset:36160
	s_waitcnt lgkmcnt(0)
	v_mfma_f32_16x16x32_bf16 v[42:45], v[84:87], v[78:81], v[42:45]
	ds_read_b64_tr_b16 v[84:85], v82 offset:44224
	ds_read_b64_tr_b16 v[86:87], v82 offset:45376
	s_waitcnt lgkmcnt(0)
	v_mfma_f32_16x16x32_bf16 v[42:45], v[84:87], v[74:77], v[42:45]
	ds_read_b128 v[84:87], v92 offset:448
	s_waitcnt lgkmcnt(0)
	v_pk_mul_f32 v[58:59], v[58:59], v[84:85]
	v_pk_mul_f32 v[60:61], v[60:61], v[86:87]
	ds_read_b64_tr_b16 v[84:85], v82 offset:35040
	ds_read_b64_tr_b16 v[86:87], v82 offset:36192
	s_waitcnt lgkmcnt(0)
	v_mfma_f32_16x16x32_bf16 v[58:61], v[84:87], v[78:81], v[58:61]
	ds_read_b64_tr_b16 v[78:79], v82 offset:44256
	ds_read_b64_tr_b16 v[80:81], v82 offset:45408
	s_waitcnt lgkmcnt(0)
	s_barrier
	s_waitcnt lgkmcnt(0)
	v_mfma_f32_16x16x32_bf16 v[58:61], v[78:81], v[74:77], v[58:61]
	ds_read_b128 v[86:89], v161
	ds_read_b128 v[82:85], v161 offset:16
	ds_read_b128 v[78:81], v161 offset:32
	ds_read_b128 v[74:77], v161 offset:48
	s_waitcnt lgkmcnt(3)
	v_pk_mul_f32 v[90:91], v[88:89], v[88:89]
	v_pk_mul_f32 v[92:93], v[86:87], v[86:87]
	s_nop 0
	v_pk_mov_b32 v[94:95], v[92:93], v[90:91] op_sel:[1,0]
	v_mov_b32_e32 v93, v91
	v_pk_add_f32 v[90:91], v[94:95], v[92:93]
	s_waitcnt lgkmcnt(2)
	v_pk_mul_f32 v[92:93], v[84:85], v[84:85]
	v_pk_mul_f32 v[94:95], v[82:83], v[82:83]
	v_pk_add_f32 v[90:91], v[90:91], v[90:91] op_sel:[0,1] op_sel_hi:[1,0]
	v_pk_mov_b32 v[96:97], v[94:95], v[92:93] op_sel:[1,0]
	v_mov_b32_e32 v95, v93
	v_pk_add_f32 v[92:93], v[96:97], v[94:95]
	s_waitcnt lgkmcnt(0)
	v_mul_f32_e32 v94, v74, v74
	v_mul_f32_e32 v95, v75, v75
	v_pk_add_f32 v[92:93], v[92:93], v[92:93] op_sel:[0,1] op_sel_hi:[1,0]
	v_mov_b32_e32 v91, v94
	v_mov_b32_e32 v93, v95
	v_pk_add_f32 v[90:91], v[90:91], v[92:93]
	v_mul_f32_e32 v92, v79, v79
	v_mul_f32_e32 v94, v81, v81
	v_mul_f32_e32 v96, v76, v76
	v_mul_f32_e32 v97, v77, v77
	v_pk_fma_f32 v[92:93], v[78:79], v[78:79], v[92:93] op_sel_hi:[1,1,0]
	v_pk_fma_f32 v[94:95], v[80:81], v[80:81], v[94:95] op_sel_hi:[1,1,0]
	v_mov_b32_e32 v93, v96
	v_mov_b32_e32 v95, v97
	v_pk_add_f32 v[92:93], v[92:93], v[94:95]
	s_nop 0
	v_pk_add_f32 v[90:91], v[90:91], v[92:93]
	v_and_b32_e32 v92, 64, v166
	v_add_f32_e32 v90, v90, v91
	v_xor_b32_e32 v91, 1, v166
	v_add_u32_e32 v92, 64, v92
	v_cmp_lt_i32_e32 vcc, v91, v92
	s_nop 1
	v_cndmask_b32_e32 v91, v166, v91, vcc
	v_lshlrev_b32_e32 v91, 2, v91
	ds_bpermute_b32 v91, v91, v90
	s_waitcnt lgkmcnt(0)
	v_add_f32_e32 v90, v90, v91
	v_xor_b32_e32 v91, 2, v166
	v_cmp_lt_i32_e32 vcc, v91, v92
	s_nop 1
	v_cndmask_b32_e32 v91, v166, v91, vcc
	v_lshlrev_b32_e32 v91, 2, v91
	ds_bpermute_b32 v91, v91, v90
	s_waitcnt lgkmcnt(0)
	v_add_f32_e32 v90, v90, v91
	v_xor_b32_e32 v91, 4, v166
	v_cmp_lt_i32_e32 vcc, v91, v92
	s_nop 1
	v_cndmask_b32_e32 v91, v166, v91, vcc
	v_lshlrev_b32_e32 v91, 2, v91
	ds_bpermute_b32 v91, v91, v90
	s_waitcnt lgkmcnt(0)
	v_add_f32_e32 v90, v90, v91
	v_fmamk_f32 v90, v90, 0x3c000000, v162
	v_cmp_gt_f32_e32 vcc, s45, v90
	v_mul_f32_e32 v91, 0x4b800000, v90
	s_nop 0
	v_cndmask_b32_e32 v90, v90, v91, vcc
	v_rsq_f32_e32 v90, v90
	s_nop 0
	v_mul_f32_e32 v91, 0x45800000, v90
	v_cndmask_b32_e32 v108, v90, v91, vcc
	v_mov_b64_e32 v[90:91], v[194:195]
	v_mov_b64_e32 v[92:93], v[196:197]
	v_mov_b64_e32 v[94:95], v[198:199]
	v_mov_b64_e32 v[96:97], v[200:201]
	v_mov_b64_e32 v[98:99], v[202:203]
	v_mov_b64_e32 v[100:101], v[204:205]
	v_mov_b64_e32 v[102:103], v[206:207]
	v_mov_b64_e32 v[104:105], v[208:209]
	v_mul_f32_e32 v86, v86, v108
	v_mul_f32_e32 v87, v87, v108
	v_mul_f32_e32 v83, v83, v108
	v_mul_f32_e32 v79, v79, v108
	v_mul_f32_e32 v74, v74, v108
	v_mul_f32_e32 v82, v82, v108
	v_mul_f32_e32 v78, v78, v108
	v_mul_f32_e32 v74, v90, v74
	v_mul_f32_e32 v79, v95, v79
	v_mul_f32_e32 v83, v99, v83
	v_mul_f32_e32 v86, v102, v86
	v_lshlrev_b32_e32 v102, 16, v46
	v_mul_f32_e32 v87, v103, v87
	v_and_b32_e32 v46, 0xffff0000, v46
	v_mul_f32_e32 v46, v87, v46
	v_mul_f32_e32 v87, v88, v108
	v_mul_f32_e32 v87, v104, v87
	v_lshlrev_b32_e32 v88, 16, v47
	v_mul_f32_e32 v87, v87, v88
	v_mul_f32_e32 v88, v89, v108
	v_mul_f32_e32 v88, v105, v88
	v_and_b32_e32 v47, 0xffff0000, v47
	v_mul_f32_e32 v47, v88, v47
	v_lshlrev_b32_e32 v88, 16, v48
	v_and_b32_e32 v48, 0xffff0000, v48
	v_mul_f32_e32 v48, v83, v48
	v_mul_f32_e32 v83, v84, v108
	v_mul_f32_e32 v83, v100, v83
	v_lshlrev_b32_e32 v84, 16, v49
	v_mul_f32_e32 v83, v83, v84
	v_mul_f32_e32 v84, v85, v108
	v_mul_f32_e32 v84, v101, v84
	v_and_b32_e32 v49, 0xffff0000, v49
	v_mul_f32_e32 v49, v84, v49
	v_lshlrev_b32_e32 v84, 16, v38
	v_and_b32_e32 v38, 0xffff0000, v38
	v_mul_f32_e32 v38, v79, v38
	v_mul_f32_e32 v79, v80, v108
	v_mul_f32_e32 v79, v96, v79
	v_lshlrev_b32_e32 v80, 16, v39
	v_mul_f32_e32 v79, v79, v80
	v_mul_f32_e32 v80, v81, v108
	v_mul_f32_e32 v80, v97, v80
	v_and_b32_e32 v39, 0xffff0000, v39
	v_mul_f32_e32 v39, v80, v39
	v_lshlrev_b32_e32 v80, 16, v40
	v_mul_f32_e32 v80, v74, v80
	v_mul_f32_e32 v74, v75, v108
	v_mul_f32_e32 v74, v91, v74
	v_and_b32_e32 v40, 0xffff0000, v40
	v_mul_f32_e32 v40, v74, v40
	v_mul_f32_e32 v74, v76, v108
	v_mul_f32_e32 v74, v92, v74
	v_lshlrev_b32_e32 v75, 16, v41
	v_mul_f32_e32 v81, v74, v75
	v_mul_f32_e32 v74, v77, v108
	v_mul_f32_e32 v82, v98, v82
	v_mul_f32_e32 v78, v94, v78
	v_mul_f32_e32 v74, v93, v74
	v_and_b32_e32 v41, 0xffff0000, v41
	v_mul_f32_e32 v86, v86, v102
	v_mul_f32_e32 v82, v82, v88
	v_mul_f32_e32 v78, v78, v84
	v_mul_f32_e32 v41, v74, v41
	v_mov_b32_e32 v74, 0
	v_mov_b32_e32 v75, 0
	v_mov_b32_e32 v76, 0
	v_mov_b32_e32 v77, 0
	v_cvt_pk_fp8_f32 v74, v86, v46
	v_cvt_pk_fp8_f32 v75, v82, v48
	v_cvt_pk_fp8_f32 v76, v78, v38
	v_cvt_pk_fp8_f32 v77, v80, v40
	v_cvt_pk_fp8_f32 v74, v87, v47 op_sel:[0,0,1]
	v_cvt_pk_fp8_f32 v75, v83, v49 op_sel:[0,0,1]
	v_cvt_pk_fp8_f32 v76, v79, v39 op_sel:[0,0,1]
	v_cvt_pk_fp8_f32 v77, v81, v41 op_sel:[0,0,1]
	v_lshlrev_b64 v[38:39], 11, v[122:123]
	v_lshl_add_u64 v[78:79], v[116:117], 0, v[38:39]
	s_cbranch_scc0 .LBB0_642
	s_waitcnt vmcnt(0)
	v_mov_b64_e32 v[38:39], v[70:71]
	v_mov_b64_e32 v[46:47], v[66:67]
	v_mov_b64_e32 v[40:41], v[72:73]
	v_mov_b64_e32 v[48:49], v[68:69]
	s_branch .LBB0_650
